# P1 inner-loop header bookkeeping hoisted into the previous MFMA run so all twelve LDS reads of phase 1 issue back to back
# baseline (speedup 1.0000x reference)
.LBB2_32:
	s_xor_b64 s[30:31], s[4:5], -1
	s_lshl_b32 s4, s63, 8
	s_ashr_i32 s5, s4, 31
	s_lshl_b64 s[4:5], s[4:5], 11
	s_add_u32 s4, s14, s4
	s_addc_u32 s5, s15, s5
	s_add_u32 s24, s4, 0x400000
	s_addc_u32 s25, s5, 0
	s_and_b64 s[4:5], s[28:29], exec
	s_cselect_b32 s66, s25, s19
	s_cselect_b32 s67, s24, s18
	s_lshl_b32 s4, s62, 8
	s_ashr_i32 s5, s4, 31
	s_lshl_b64 s[4:5], s[4:5], 11
	s_add_u32 s26, s12, s4
	s_addc_u32 s27, s13, s5
	s_and_b64 s[4:5], s[28:29], exec
	s_cselect_b32 s68, s27, s1
	s_cselect_b32 s69, s26, s0
	s_add_u32 s70, s18, 0x40080
	s_addc_u32 s71, s19, 0
	s_add_u32 s72, s0, 0x100
	v_mov_b64_e32 v[0:1], 0
	s_addc_u32 s73, s1, 0
	s_mov_b32 s74, -2
	v_mov_b64_e32 v[2:3], 0
	v_mov_b64_e32 v[4:5], 0
	v_mov_b64_e32 v[6:7], 0
	v_mov_b64_e32 v[8:9], 0
	v_mov_b64_e32 v[10:11], 0
	v_mov_b64_e32 v[12:13], 0
	v_mov_b64_e32 v[14:15], 0
	v_mov_b64_e32 v[16:17], 0
	v_mov_b64_e32 v[18:19], 0
	v_mov_b64_e32 v[20:21], 0
	v_mov_b64_e32 v[22:23], 0
	v_mov_b64_e32 v[24:25], 0
	v_mov_b64_e32 v[26:27], 0
	v_mov_b64_e32 v[28:29], 0
	v_mov_b64_e32 v[30:31], 0
	v_mov_b64_e32 v[32:33], 0
	v_mov_b64_e32 v[34:35], 0
	v_mov_b64_e32 v[36:37], 0
	v_mov_b64_e32 v[38:39], 0
	v_mov_b64_e32 v[40:41], 0
	v_mov_b64_e32 v[42:43], 0
	v_mov_b64_e32 v[44:45], 0
	v_mov_b64_e32 v[46:47], 0
	v_mov_b64_e32 v[48:49], 0
	v_mov_b64_e32 v[50:51], 0
	v_mov_b64_e32 v[52:53], 0
	v_mov_b64_e32 v[54:55], 0
	v_mov_b64_e32 v[56:57], 0
	v_mov_b64_e32 v[58:59], 0
	v_mov_b64_e32 v[60:61], 0
	v_mov_b64_e32 v[62:63], 0
	v_mov_b64_e32 v[64:65], 0
	v_mov_b64_e32 v[66:67], 0
	v_mov_b64_e32 v[68:69], 0
	v_mov_b64_e32 v[70:71], 0
	v_mov_b64_e32 v[72:73], 0
	v_mov_b64_e32 v[74:75], 0
	v_mov_b64_e32 v[76:77], 0
	v_mov_b64_e32 v[78:79], 0
	v_mov_b64_e32 v[80:81], 0
	v_mov_b64_e32 v[82:83], 0
	v_mov_b64_e32 v[84:85], 0
	v_mov_b64_e32 v[86:87], 0
	v_mov_b64_e32 v[88:89], 0
	v_mov_b64_e32 v[90:91], 0
	v_mov_b64_e32 v[92:93], 0
	v_mov_b64_e32 v[94:95], 0
	v_mov_b64_e32 v[96:97], 0
	v_mov_b64_e32 v[98:99], 0
	v_mov_b64_e32 v[100:101], 0
	v_mov_b64_e32 v[102:103], 0
	v_mov_b64_e32 v[104:105], 0
	v_mov_b64_e32 v[106:107], 0
	v_mov_b64_e32 v[108:109], 0
	v_mov_b64_e32 v[110:111], 0
	v_mov_b64_e32 v[112:113], 0
	v_mov_b64_e32 v[114:115], 0
	v_mov_b64_e32 v[116:117], 0
	v_mov_b64_e32 v[118:119], 0
	v_mov_b64_e32 v[120:121], 0
	v_mov_b64_e32 v[122:123], 0
	v_mov_b64_e32 v[124:125], 0
	v_mov_b64_e32 v[126:127], 0
	s_waitcnt lgkmcnt(0)
	s_cmp_lg_u32 s74, 12
	s_cselect_b64 s[0:1], -1, 0
	s_and_b64 s[4:5], s[0:1], exec
	s_cselect_b32 s75, s73, s68
	s_cselect_b32 s16, s72, s69
	s_and_b32 s5, s71, 0xffff
	s_mov_b32 s4, s70
	s_or_b64 s[36:37], s[28:29], s[0:1]
	v_add_u32_e32 v212, 0x1c000, v199
	v_add_u32_e32 v213, 0x1c000, v200
	s_branch .LBB2_34

.LBB2_34:
	ds_read_b128 v[144:147], v203
	ds_read_b128 v[148:151], v203 offset:2048
	ds_read_b128 v[156:159], v204
	ds_read_b128 v[152:155], v204 offset:2048
	s_mov_b32 m0, s53
	ds_read_b128 v[184:187], v205
	ds_read_b128 v[172:175], v205 offset:2048
	ds_read_b128 v[188:191], v206
	ds_read_b128 v[176:179], v206 offset:2048
	ds_read_b128 v[168:171], v205 offset:4096
	ds_read_b128 v[160:163], v205 offset:6144
	ds_read_b128 v[180:183], v206 offset:4096
	ds_read_b128 v[164:167], v206 offset:6144
	buffer_load_dwordx4 v193, s[4:7], 0 offen lds
	s_mov_b32 m0, s54
	s_nop 0
	buffer_load_dwordx4 v197, s[4:7], 0 offen lds
	s_waitcnt lgkmcnt(8)
	s_barrier
	s_waitcnt lgkmcnt(0)
	s_setprio 1
	v_mfma_i32_16x16x64_i8 v[124:127], v[144:147], v[184:187], v[124:127]
	s_xor_b64 s[34:35], s[36:37], -1
	v_mfma_i32_16x16x64_i8 v[120:123], v[148:151], v[184:187], v[120:123]
	v_mfma_i32_16x16x64_i8 v[108:111], v[144:147], v[172:175], v[108:111]
	v_mfma_i32_16x16x64_i8 v[104:107], v[148:151], v[172:175], v[104:107]
	v_mfma_i32_16x16x64_i8 v[96:99], v[144:147], v[168:171], v[96:99]
	v_mfma_i32_16x16x64_i8 v[88:91], v[148:151], v[168:171], v[88:91]
	v_mfma_i32_16x16x64_i8 v[80:83], v[144:147], v[160:163], v[80:83]
	v_mfma_i32_16x16x64_i8 v[72:75], v[148:151], v[160:163], v[72:75]
	v_mfma_i32_16x16x64_i8 v[124:127], v[156:159], v[188:191], v[124:127]
	v_mfma_i32_16x16x64_i8 v[120:123], v[152:155], v[188:191], v[120:123]
	v_mfma_i32_16x16x64_i8 v[108:111], v[156:159], v[176:179], v[108:111]
	v_mfma_i32_16x16x64_i8 v[104:107], v[152:155], v[176:179], v[104:107]
	v_mfma_i32_16x16x64_i8 v[96:99], v[156:159], v[180:183], v[96:99]
	v_mfma_i32_16x16x64_i8 v[88:91], v[152:155], v[180:183], v[88:91]
	v_mfma_i32_16x16x64_i8 v[80:83], v[156:159], v[164:167], v[80:83]
	v_mfma_i32_16x16x64_i8 v[72:75], v[152:155], v[164:167], v[72:75]
	s_setprio 0
	s_barrier
	ds_read_b128 v[128:131], v207
	ds_read_b128 v[132:135], v207 offset:2048
	ds_read_b128 v[140:143], v208
	ds_read_b128 v[136:139], v208 offset:2048
	s_and_b64 vcc, exec, s[34:35]
	s_cbranch_vccnz .LBB2_36
	s_and_b32 s17, s75, 0xffff
	s_mov_b32 s18, s6
	s_mov_b32 s19, s7
	s_mov_b32 m0, s39
	s_nop 0
	buffer_load_dwordx4 v196, s[16:19], 0 offen lds
	s_mov_b32 m0, s40
	s_nop 0
	buffer_load_dwordx4 v198, s[16:19], 0 offen lds
